# combination variant with two more DPP wave reductions (N1 combine variant and MoE N2 amax)
# speedup vs baseline: 1.0112x; 1.0031x over previous
.LBB0_399:
	v_readlane_b32 s40, v251, 5
	v_readlane_b32 s46, v251, 11
	v_readlane_b32 s47, v251, 12
	s_mov_b32 s0, 0xf800000
	s_mov_b32 s3, 0x42fe0000
	v_lshl_add_u64 v[68:69], s[46:47], 0, v[88:89]
	v_add_co_u32_e32 v106, vcc, 0x500000, v68
	v_readlane_b32 s41, v251, 6
	s_nop 0
	v_addc_co_u32_e32 v107, vcc, 0, v69, vcc
	global_load_dwordx2 v[68:69], v[106:107], off
	global_load_dwordx2 v[70:71], v[106:107], off offset:512
	global_load_dwordx2 v[98:99], v[106:107], off offset:1024
	global_load_dwordx2 v[112:113], v[106:107], off offset:1536
	v_readlane_b32 s42, v251, 7
	v_readlane_b32 s43, v251, 8
	v_readlane_b32 s44, v251, 9
	v_readlane_b32 s45, v251, 10
	s_waitcnt vmcnt(3)
	v_lshlrev_b32_e32 v108, 16, v68
	v_and_b32_e32 v109, 0xffff0000, v68
	v_lshlrev_b32_e32 v96, 16, v69
	v_and_b32_e32 v97, 0xffff0000, v69
	v_lshl_add_u64 v[68:69], s[46:47], 0, v[84:85]
	s_waitcnt vmcnt(2)
	v_lshlrev_b32_e32 v94, 16, v70
	v_and_b32_e32 v95, 0xffff0000, v70
	v_lshlrev_b32_e32 v110, 16, v71
	v_and_b32_e32 v111, 0xffff0000, v71
	global_load_dwordx4 v[68:71], v[68:69], off
	s_waitcnt vmcnt(0)
	v_lshl_add_u64 v[68:69], s[46:47], 0, v[86:87]
	global_load_dwordx2 v[68:69], v[68:69], off
	v_lshlrev_b32_e32 v104, 16, v98
	v_and_b32_e32 v105, 0xffff0000, v98
	v_lshlrev_b32_e32 v102, 16, v99
	v_and_b32_e32 v103, 0xffff0000, v99
	v_lshlrev_b32_e32 v100, 16, v112
	v_and_b32_e32 v101, 0xffff0000, v112
	v_lshlrev_b32_e32 v98, 16, v113
	v_and_b32_e32 v99, 0xffff0000, v113
	v_mov_b32_e32 v128, v71
	s_waitcnt vmcnt(0)
	v_ashrrev_i32_e32 v113, 31, v68
	v_mov_b32_e32 v112, v68
	v_lshlrev_b64 v[112:113], 11, v[112:113]
	v_ashrrev_i32_e32 v115, 31, v69
	v_mov_b32_e32 v114, v69
	v_lshl_add_u64 v[112:113], v[82:83], 0, v[112:113]
	v_lshlrev_b64 v[68:69], 11, v[114:115]
	v_lshl_add_u64 v[114:115], v[82:83], 0, v[68:69]
	global_load_dwordx2 v[68:69], v[112:113], off
	global_load_dwordx2 v[122:123], v[114:115], off
	s_waitcnt vmcnt(1)
	v_lshlrev_b32_e32 v124, 16, v68
	s_waitcnt vmcnt(0)
	v_lshlrev_b32_e32 v126, 16, v122
	v_and_b32_e32 v127, 0xffff0000, v122
	v_lshlrev_b32_e32 v122, 16, v123
	v_and_b32_e32 v123, 0xffff0000, v123
	v_and_b32_e32 v125, 0xffff0000, v68
	v_lshlrev_b32_e32 v68, 16, v69
	v_and_b32_e32 v69, 0xffff0000, v69
	v_pk_mul_f32 v[122:123], v[128:129], v[122:123] op_sel_hi:[0,1]
	v_pk_mul_f32 v[126:127], v[128:129], v[126:127] op_sel_hi:[0,1]
	v_pk_fma_f32 v[124:125], v[70:71], v[124:125], v[126:127] op_sel_hi:[0,1,1]
	v_pk_fma_f32 v[68:69], v[70:71], v[68:69], v[122:123] op_sel_hi:[0,1,1]
	v_pk_fma_f32 v[96:97], v[64:65], v[68:69], v[96:97]
	v_pk_fma_f32 v[108:109], v[62:63], v[124:125], v[108:109]
	v_cvt_pk_bf16_f32 v69, v96, v97
	v_cvt_pk_bf16_f32 v68, v108, v109
	global_store_dwordx2 v[106:107], v[68:69], off
	global_load_dwordx2 v[68:69], v[112:113], off offset:512
	s_nop 0
	global_load_dwordx2 v[122:123], v[114:115], off offset:512
	s_waitcnt vmcnt(1)
	v_lshlrev_b32_e32 v124, 16, v68
	s_waitcnt vmcnt(0)
	v_lshlrev_b32_e32 v126, 16, v122
	v_and_b32_e32 v127, 0xffff0000, v122
	v_lshlrev_b32_e32 v122, 16, v123
	v_and_b32_e32 v123, 0xffff0000, v123
	v_and_b32_e32 v125, 0xffff0000, v68
	v_lshlrev_b32_e32 v68, 16, v69
	v_and_b32_e32 v69, 0xffff0000, v69
	v_pk_mul_f32 v[122:123], v[128:129], v[122:123] op_sel_hi:[0,1]
	v_pk_mul_f32 v[126:127], v[128:129], v[126:127] op_sel_hi:[0,1]
	v_pk_fma_f32 v[124:125], v[70:71], v[124:125], v[126:127] op_sel_hi:[0,1,1]
	v_pk_fma_f32 v[68:69], v[70:71], v[68:69], v[122:123] op_sel_hi:[0,1,1]
	v_pk_fma_f32 v[68:69], v[56:57], v[68:69], v[110:111]
	v_pk_fma_f32 v[94:95], v[54:55], v[124:125], v[94:95]
	v_cvt_pk_bf16_f32 v111, v68, v69
	v_cvt_pk_bf16_f32 v110, v94, v95
	global_store_dwordx2 v[106:107], v[110:111], off offset:512
	global_load_dwordx2 v[110:111], v[112:113], off offset:1024
	s_nop 0
	global_load_dwordx2 v[122:123], v[114:115], off offset:1024
	s_waitcnt vmcnt(1)
	v_lshlrev_b32_e32 v124, 16, v110
	s_waitcnt vmcnt(0)
	v_lshlrev_b32_e32 v126, 16, v122
	v_and_b32_e32 v127, 0xffff0000, v122
	v_lshlrev_b32_e32 v122, 16, v123
	v_and_b32_e32 v123, 0xffff0000, v123
	v_and_b32_e32 v125, 0xffff0000, v110
	v_lshlrev_b32_e32 v110, 16, v111
	v_and_b32_e32 v111, 0xffff0000, v111
	v_pk_mul_f32 v[122:123], v[128:129], v[122:123] op_sel_hi:[0,1]
	v_pk_mul_f32 v[126:127], v[128:129], v[126:127] op_sel_hi:[0,1]
	v_pk_fma_f32 v[124:125], v[70:71], v[124:125], v[126:127] op_sel_hi:[0,1,1]
	v_pk_fma_f32 v[110:111], v[70:71], v[110:111], v[122:123] op_sel_hi:[0,1,1]
	v_pk_fma_f32 v[102:103], v[52:53], v[110:111], v[102:103]
	v_pk_fma_f32 v[104:105], v[50:51], v[124:125], v[104:105]
	v_cvt_pk_bf16_f32 v111, v102, v103
	v_cvt_pk_bf16_f32 v110, v104, v105
	global_store_dwordx2 v[106:107], v[110:111], off offset:1024
	global_load_dwordx2 v[110:111], v[112:113], off offset:1536
	s_nop 0
	global_load_dwordx2 v[112:113], v[114:115], off offset:1536
	s_waitcnt vmcnt(1)
	v_lshlrev_b32_e32 v114, 16, v110
	s_waitcnt vmcnt(0)
	v_lshlrev_b32_e32 v122, 16, v112
	v_and_b32_e32 v123, 0xffff0000, v112
	v_lshlrev_b32_e32 v112, 16, v113
	v_and_b32_e32 v113, 0xffff0000, v113
	v_and_b32_e32 v115, 0xffff0000, v110
	v_lshlrev_b32_e32 v110, 16, v111
	v_and_b32_e32 v111, 0xffff0000, v111
	v_pk_mul_f32 v[112:113], v[128:129], v[112:113] op_sel_hi:[0,1]
	v_pk_mul_f32 v[122:123], v[128:129], v[122:123] op_sel_hi:[0,1]
	v_pk_fma_f32 v[114:115], v[70:71], v[114:115], v[122:123] op_sel_hi:[0,1,1]
	v_pk_fma_f32 v[70:71], v[70:71], v[110:111], v[112:113] op_sel_hi:[0,1,1]
	v_pk_fma_f32 v[98:99], v[60:61], v[70:71], v[98:99]
	v_pk_fma_f32 v[100:101], v[58:59], v[114:115], v[100:101]
	v_cvt_pk_bf16_f32 v71, v98, v99
	v_cvt_pk_bf16_f32 v70, v100, v101
	global_store_dwordx2 v[106:107], v[70:71], off offset:1536
	v_pk_mul_f32 v[70:71], v[96:97], v[96:97]
	v_pk_mul_f32 v[106:107], v[108:109], v[108:109]
	s_nop 0
	v_pk_mov_b32 v[110:111], v[106:107], v[70:71] op_sel:[1,0]
	v_mov_b32_e32 v107, v71
	v_pk_add_f32 v[70:71], v[110:111], v[106:107]
	v_pk_mul_f32 v[106:107], v[68:69], v[68:69]
	v_pk_mul_f32 v[110:111], v[94:95], v[94:95]
	v_pk_add_f32 v[70:71], v[70:71], v[70:71] op_sel:[0,1] op_sel_hi:[1,0]
	v_pk_mov_b32 v[112:113], v[110:111], v[106:107] op_sel:[1,0]
	v_mov_b32_e32 v111, v107
	v_pk_add_f32 v[106:107], v[112:113], v[110:111]
	v_mul_f32_e32 v110, v100, v100
	v_mul_f32_e32 v111, v101, v101
	v_pk_add_f32 v[106:107], v[106:107], v[106:107] op_sel:[0,1] op_sel_hi:[1,0]
	v_mov_b32_e32 v71, v110
	v_mov_b32_e32 v107, v111
	v_pk_add_f32 v[70:71], v[70:71], v[106:107]
	v_mul_f32_e32 v106, v105, v105
	v_mul_f32_e32 v110, v103, v103
	v_mul_f32_e32 v112, v98, v98
	v_mul_f32_e32 v113, v99, v99
	v_pk_fma_f32 v[106:107], v[104:105], v[104:105], v[106:107] op_sel_hi:[1,1,0]
	v_pk_fma_f32 v[110:111], v[102:103], v[102:103], v[110:111] op_sel_hi:[1,1,0]
	v_mov_b32_e32 v107, v112
	v_mov_b32_e32 v111, v113
	v_pk_add_f32 v[106:107], v[106:107], v[110:111]
	s_nop 0
	v_pk_add_f32 v[70:71], v[70:71], v[106:107]
	s_nop 0
	v_add_f32_e32 v70, v70, v71
	s_waitcnt lgkmcnt(0)
	s_nop 1
	v_add_f32_dpp v70, v70, v70 quad_perm:[1,0,3,2] row_mask:0xf bank_mask:0xf
	s_nop 1
	v_add_f32_dpp v70, v70, v70 quad_perm:[2,3,0,1] row_mask:0xf bank_mask:0xf
	s_nop 1
	v_add_f32_dpp v70, v70, v70 row_half_mirror row_mask:0xf bank_mask:0xf
	s_nop 1
	v_add_f32_dpp v70, v70, v70 row_mirror row_mask:0xf bank_mask:0xf
	s_nop 1
	v_readlane_b32 s98, v70, 0
	v_readlane_b32 s99, v70, 16
	v_readlane_b32 s100, v70, 32
	v_readlane_b32 s101, v70, 48
	s_nop 1
	v_mov_b32_e32 v71, s99
	v_add_f32_e32 v71, s98, v71
	v_mov_b32_e32 v70, s101
	v_add_f32_e32 v70, s100, v70
	v_add_f32_e32 v70, v71, v70
	v_fmamk_f32 v70, v70, 0x3a800000, v241
	v_cmp_gt_f32_e32 vcc, s0, v70
	v_mul_f32_e32 v71, 0x4f800000, v70
	s_nop 0
	v_cndmask_b32_e32 v70, v70, v71, vcc
	v_sqrt_f32_e32 v71, v70
	s_nop 0
	v_add_u32_e32 v106, -1, v71
	v_fma_f32 v107, -v106, v71, v70
	v_cmp_ge_f32_e64 s[0:1], 0, v107
	v_add_u32_e32 v107, 1, v71
	s_nop 0
	v_cndmask_b32_e64 v106, v71, v106, s[0:1]
	v_fma_f32 v71, -v107, v71, v70
	v_cmp_lt_f32_e64 s[0:1], 0, v71
	s_nop 1
	v_cndmask_b32_e64 v71, v106, v107, s[0:1]
	v_mul_f32_e32 v106, 0x37800000, v71
	v_cndmask_b32_e32 v71, v71, v106, vcc
	v_cmp_class_f32_e32 vcc, v70, v188
	s_nop 1
	v_cndmask_b32_e32 v70, v71, v70, vcc
	v_div_scale_f32 v71, s[0:1], v70, v70, 1.0
	v_rcp_f32_e32 v106, v71
	s_nop 0
	v_fma_f32 v107, -v71, v106, 1.0
	v_fmac_f32_e32 v106, v107, v106
	v_div_scale_f32 v107, vcc, 1.0, v70, 1.0
	v_mul_f32_e32 v110, v107, v106
	v_fma_f32 v111, -v71, v110, v107
	v_fmac_f32_e32 v110, v111, v106
	v_fma_f32 v71, -v71, v110, v107
	v_div_fmas_f32 v71, v71, v106, v110
	v_div_fixup_f32 v110, v71, v70, 1.0
	v_pk_mul_f32 v[70:71], v[96:97], v[110:111] op_sel_hi:[1,0]
	v_pk_add_f32 v[106:107], v[20:21], 1.0 op_sel_hi:[1,0]
	v_pk_mul_f32 v[70:71], v[16:17], v[70:71]
	v_pk_mul_f32 v[96:97], v[108:109], v[110:111] op_sel_hi:[1,0]
	v_pk_fma_f32 v[106:107], v[106:107], v[70:71], v[40:41]
	v_pk_mul_f32 v[68:69], v[68:69], v[110:111] op_sel_hi:[1,0]
	v_pk_mul_f32 v[70:71], v[94:95], v[110:111] op_sel_hi:[1,0]
	v_pk_mul_f32 v[96:97], v[14:15], v[96:97]
	v_pk_add_f32 v[108:109], v[18:19], 1.0 op_sel_hi:[1,0]
	v_pk_mul_f32 v[94:95], v[10:11], v[70:71]
	v_pk_mul_f32 v[68:69], v[12:13], v[68:69]
	v_pk_add_f32 v[70:71], v[24:25], 1.0 op_sel_hi:[1,0]
	v_pk_fma_f32 v[108:109], v[108:109], v[96:97], v[38:39]
	v_pk_add_f32 v[96:97], v[22:23], 1.0 op_sel_hi:[1,0]
	v_pk_fma_f32 v[70:71], v[70:71], v[68:69], v[36:37]
	v_pk_mul_f32 v[68:69], v[102:103], v[110:111] op_sel_hi:[1,0]
	v_pk_fma_f32 v[96:97], v[96:97], v[94:95], v[34:35]
	v_pk_mul_f32 v[94:95], v[104:105], v[110:111] op_sel_hi:[1,0]
	v_pk_mul_f32 v[68:69], v[8:9], v[68:69]
	v_pk_add_f32 v[102:103], v[32:33], 1.0 op_sel_hi:[1,0]
	v_pk_mul_f32 v[98:99], v[98:99], v[110:111] op_sel_hi:[1,0]
	v_pk_mul_f32 v[94:95], v[6:7], v[94:95]
	v_pk_add_f32 v[104:105], v[30:31], 1.0 op_sel_hi:[1,0]
	v_pk_fma_f32 v[68:69], v[102:103], v[68:69], v[44:45]
	v_pk_mul_f32 v[100:101], v[100:101], v[110:111] op_sel_hi:[1,0]
	v_pk_mul_f32 v[98:99], v[4:5], v[98:99]
	v_pk_add_f32 v[102:103], v[28:29], 1.0 op_sel_hi:[1,0]
	v_pk_fma_f32 v[94:95], v[104:105], v[94:95], v[42:43]
	v_pk_mul_f32 v[100:101], v[2:3], v[100:101]
	v_pk_add_f32 v[104:105], v[26:27], 1.0 op_sel_hi:[1,0]
	v_pk_fma_f32 v[98:99], v[102:103], v[98:99], v[48:49]
	v_max_f32_e64 v102, |v108|, |v109|
	v_max_f32_e64 v103, |v106|, |v107|
	v_pk_fma_f32 v[100:101], v[104:105], v[100:101], v[46:47]
	v_max3_f32 v102, v102, 0, v103
	v_max_f32_e64 v103, |v96|, |v97|
	v_max_f32_e64 v104, |v70|, |v71|
	v_max3_f32 v102, v102, v103, v104
	v_max_f32_e64 v103, |v94|, |v95|
	v_max_f32_e64 v104, |v68|, |v69|
	v_max3_f32 v102, v102, v103, v104
	v_max_f32_e64 v103, |v100|, |v101|
	v_max_f32_e64 v104, |v98|, |v99|
	v_max3_f32 v102, v102, v103, v104
	s_waitcnt lgkmcnt(0)
	s_nop 1
	v_max_f32_dpp v102, v102, v102 quad_perm:[1,0,3,2] row_mask:0xf bank_mask:0xf
	s_nop 1
	v_max_f32_dpp v102, v102, v102 quad_perm:[2,3,0,1] row_mask:0xf bank_mask:0xf
	s_nop 1
	v_max_f32_dpp v102, v102, v102 row_half_mirror row_mask:0xf bank_mask:0xf
	s_nop 1
	v_max_f32_dpp v102, v102, v102 row_mirror row_mask:0xf bank_mask:0xf
	s_nop 1
	v_readlane_b32 s98, v102, 0
	v_readlane_b32 s99, v102, 16
	v_readlane_b32 s100, v102, 32
	v_readlane_b32 s101, v102, 48
	s_nop 1
	v_mov_b32_e32 v103, s99
	v_max_f32_e32 v103, s98, v103
	v_mov_b32_e32 v102, s101
	v_max_f32_e32 v102, s100, v102
	v_max_f32_e32 v104, v103, v102
	v_div_scale_f32 v102, s[10:11], v104, v104, s3
	v_rcp_f32_e32 v103, v102
	v_cmp_lt_f32_e64 s[0:1], 0, v104
	v_fma_f32 v105, -v102, v103, 1.0
	v_fmac_f32_e32 v103, v105, v103
	v_div_scale_f32 v105, vcc, s3, v104, s3
	v_mul_f32_e32 v110, v105, v103
	v_fma_f32 v111, -v102, v110, v105
	v_fmac_f32_e32 v110, v111, v103
	v_fma_f32 v102, -v102, v110, v105
	v_div_fmas_f32 v102, v102, v103, v110
	v_div_fixup_f32 v102, v102, v104, s3
	v_cndmask_b32_e64 v105, 0, v102, s[0:1]
	v_mul_f32_e32 v97, v97, v105
	v_mul_f32_e32 v96, v96, v105
	v_rndne_f32_e32 v97, v97
	v_mul_f32_e32 v70, v70, v105
	v_mul_f32_e32 v71, v71, v105
	v_rndne_f32_e32 v96, v96
	v_cvt_i32_f32_e32 v97, v97
	v_rndne_f32_e32 v70, v70
	v_rndne_f32_e32 v71, v71
	v_cvt_i32_f32_e32 v96, v96
	v_cvt_i32_f32_sdwa v70, v70 dst_sel:WORD_1 dst_unused:UNUSED_PAD src0_sel:DWORD
	v_cvt_i32_f32_e32 v71, v71
	v_lshl_add_u64 v[102:103], s[46:47], 0, v[90:91]
	s_mov_b32 s0, 0x40c0c00
	s_mov_b32 s1, 0x8900000
	v_lshlrev_b32_e32 v97, 8, v97
	v_add_co_u32_e32 v102, vcc, s1, v102
	v_and_b32_e32 v97, 0xff00, v97
	v_and_b32_e32 v70, 0xff0000, v70
	v_perm_b32 v71, v71, v96, s0
	v_addc_co_u32_e32 v103, vcc, 0, v103, vcc
	v_or3_b32 v70, v71, v97, v70
	v_mul_f32_e32 v71, v95, v105
	global_store_dword v[102:103], v70, off offset:256
	v_mul_f32_e32 v70, v94, v105
	v_rndne_f32_e32 v71, v71
	v_mul_f32_e32 v68, v68, v105
	v_mul_f32_e32 v69, v69, v105
	v_rndne_f32_e32 v70, v70
	v_cvt_i32_f32_e32 v71, v71
	v_rndne_f32_e32 v68, v68
	v_rndne_f32_e32 v69, v69
	v_cvt_i32_f32_e32 v70, v70
	v_cvt_i32_f32_sdwa v68, v68 dst_sel:WORD_1 dst_unused:UNUSED_PAD src0_sel:DWORD
	v_cvt_i32_f32_e32 v69, v69
	v_lshlrev_b32_e32 v71, 8, v71
	v_and_b32_e32 v71, 0xff00, v71
	v_and_b32_e32 v68, 0xff0000, v68
	v_perm_b32 v69, v69, v70, s0
	v_mul_f32_e32 v109, v109, v105
	v_or3_b32 v68, v69, v71, v68
	v_mul_f32_e32 v69, v101, v105
	v_mul_f32_e32 v108, v108, v105
	v_rndne_f32_e32 v109, v109
	v_mul_f32_e32 v106, v106, v105
	v_mul_f32_e32 v107, v107, v105
	global_store_dword v[102:103], v68, off offset:512
	v_mul_f32_e32 v68, v100, v105
	v_rndne_f32_e32 v69, v69
	v_mul_f32_e32 v70, v98, v105
	v_mul_f32_e32 v71, v99, v105
	v_rndne_f32_e32 v108, v108
	v_cvt_i32_f32_e32 v109, v109
	v_rndne_f32_e32 v106, v106
	v_rndne_f32_e32 v107, v107
	v_rndne_f32_e32 v68, v68
	v_cvt_i32_f32_e32 v69, v69
	v_rndne_f32_e32 v70, v70
	v_rndne_f32_e32 v71, v71
	v_cvt_i32_f32_e32 v108, v108
	v_cvt_i32_f32_sdwa v106, v106 dst_sel:WORD_1 dst_unused:UNUSED_PAD src0_sel:DWORD
	v_cvt_i32_f32_e32 v107, v107
	v_cvt_i32_f32_e32 v68, v68
	v_cvt_i32_f32_sdwa v70, v70 dst_sel:WORD_1 dst_unused:UNUSED_PAD src0_sel:DWORD
	v_cvt_i32_f32_e32 v71, v71
	v_lshlrev_b32_e32 v109, 8, v109
	v_lshlrev_b32_e32 v69, 8, v69
	v_and_b32_e32 v109, 0xff00, v109
	v_and_b32_e32 v106, 0xff0000, v106
	v_perm_b32 v107, v107, v108, s0
	v_and_b32_e32 v69, 0xff00, v69
	v_and_b32_e32 v70, 0xff0000, v70
	v_perm_b32 v68, v71, v68, s0
	v_or3_b32 v106, v107, v109, v106
	v_or3_b32 v68, v68, v69, v70
	global_store_dword v[102:103], v106, off
	global_store_dword v[102:103], v68, off offset:768
	s_and_saveexec_b64 s[0:1], s[36:37]
	s_cbranch_execz .LBB0_396
	v_readlane_b32 s40, v251, 5
	v_readlane_b32 s46, v251, 11
	v_readlane_b32 s47, v251, 12
	v_mul_f32_e32 v70, 0x3c010204, v104
	v_readlane_b32 s41, v251, 6
	v_lshl_add_u64 v[68:69], s[46:47], 0, v[92:93]
	v_readlane_b32 s42, v251, 7
	v_readlane_b32 s43, v251, 8
	v_readlane_b32 s44, v251, 9
	v_readlane_b32 s45, v251, 10
	global_store_dword v[68:69], v70, off
	s_branch .LBB0_396

.LBB0_1217:
	global_load_dwordx2 v[184:185], v[198:199], off offset:-1024
	global_load_dwordx2 v[186:187], v[198:199], off offset:-512
	global_load_dwordx2 v[206:207], v[198:199], off
	global_load_dwordx2 v[208:209], v[198:199], off offset:512
	s_mov_b32 s0, 0xf800000
	s_mov_b32 s10, 0x42fe0000
	s_waitcnt vmcnt(2) lgkmcnt(3)
	v_and_b32_e32 v215, 0xffff0000, v187
	v_and_b32_e32 v214, 0xffff0000, v186
	s_waitcnt vmcnt(0) lgkmcnt(0)
	v_lshlrev_b32_e32 v221, 16, v208
	v_and_b32_e32 v219, 0xffff0000, v208
	v_lshlrev_b32_e32 v222, 16, v209
	v_and_b32_e32 v223, 0xffff0000, v209
	v_lshlrev_b32_e32 v208, 16, v184
	v_and_b32_e32 v209, 0xffff0000, v184
	v_lshlrev_b32_e32 v184, 16, v185
	v_and_b32_e32 v185, 0xffff0000, v185
	v_mul_f32_e32 v210, v185, v185
	v_pk_fma_f32 v[228:229], v[184:185], v[184:185], v[210:211] op_sel_hi:[1,1,0]
	v_lshlrev_b32_e32 v210, 16, v206
	v_and_b32_e32 v211, 0xffff0000, v206
	v_mul_f32_e32 v206, v209, v209
	v_lshlrev_b32_e32 v213, 16, v187
	v_lshlrev_b32_e32 v212, 16, v186
	v_pk_mul_f32 v[186:187], v[214:215], v[214:215]
	v_lshlrev_b32_e32 v216, 16, v207
	v_and_b32_e32 v217, 0xffff0000, v207
	v_pk_fma_f32 v[206:207], v[208:209], v[208:209], v[206:207] op_sel_hi:[1,1,0]
	v_pk_fma_f32 v[186:187], v[212:213], v[212:213], v[186:187]
	v_mov_b32_e32 v220, v206
	v_mov_b32_e32 v230, v228
	v_mov_b32_e32 v231, v221
	v_mul_f32_e32 v218, v219, v219
	v_pk_add_f32 v[206:207], v[206:207], v[228:229]
	v_pk_mul_f32 v[228:229], v[220:221], v[230:231]
	v_pk_add_f32 v[186:187], v[186:187], v[186:187] op_sel:[0,1] op_sel_hi:[1,0]
	v_mov_b32_e32 v207, v229
	v_mov_b32_e32 v187, v218
	v_pk_add_f32 v[186:187], v[206:207], v[186:187]
	v_mul_f32_e32 v206, v211, v211
	v_mul_f32_e32 v218, v217, v217
	v_mul_f32_e32 v227, v222, v222
	v_mul_f32_e32 v232, v223, v223
	v_pk_fma_f32 v[206:207], v[210:211], v[210:211], v[206:207] op_sel_hi:[1,1,0]
	v_pk_fma_f32 v[228:229], v[216:217], v[216:217], v[218:219] op_sel_hi:[1,1,0]
	v_mov_b32_e32 v207, v227
	v_mov_b32_e32 v229, v232
	v_pk_add_f32 v[206:207], v[206:207], v[228:229]
	s_nop 0
	v_pk_add_f32 v[186:187], v[186:187], v[206:207]
	s_nop 0
	v_add_f32_e32 v186, v186, v187
	s_waitcnt lgkmcnt(0)
	s_nop 1
	v_add_f32_dpp v186, v186, v186 quad_perm:[1,0,3,2] row_mask:0xf bank_mask:0xf
	s_nop 1
	v_add_f32_dpp v186, v186, v186 quad_perm:[2,3,0,1] row_mask:0xf bank_mask:0xf
	s_nop 1
	v_add_f32_dpp v186, v186, v186 row_half_mirror row_mask:0xf bank_mask:0xf
	s_nop 1
	v_add_f32_dpp v186, v186, v186 row_mirror row_mask:0xf bank_mask:0xf
	s_nop 1
	v_readlane_b32 s98, v186, 0
	v_readlane_b32 s99, v186, 16
	v_readlane_b32 s100, v186, 32
	v_readlane_b32 s101, v186, 48
	s_nop 1
	v_mov_b32_e32 v187, s99
	v_add_f32_e32 v187, s98, v187
	v_mov_b32_e32 v186, s101
	v_add_f32_e32 v186, s100, v186
	v_add_f32_e32 v186, v187, v186
	v_fmamk_f32 v186, v186, 0x3a800000, v241
	v_cmp_gt_f32_e32 vcc, s0, v186
	v_mul_f32_e32 v187, 0x4f800000, v186
	s_nop 0
	v_cndmask_b32_e32 v186, v186, v187, vcc
	v_sqrt_f32_e32 v187, v186
	s_nop 0
	v_add_u32_e32 v206, -1, v187
	v_fma_f32 v207, -v206, v187, v186
	v_cmp_ge_f32_e64 s[0:1], 0, v207
	v_add_u32_e32 v207, 1, v187
	s_nop 0
	v_cndmask_b32_e64 v206, v187, v206, s[0:1]
	v_fma_f32 v187, -v207, v187, v186
	v_cmp_lt_f32_e64 s[0:1], 0, v187
	s_nop 1
	v_cndmask_b32_e64 v187, v206, v207, s[0:1]
	v_mul_f32_e32 v206, 0x37800000, v187
	v_cndmask_b32_e32 v187, v187, v206, vcc
	v_cmp_class_f32_e32 vcc, v186, v188
	s_nop 1
	v_cndmask_b32_e32 v186, v187, v186, vcc
	v_div_scale_f32 v187, s[0:1], v186, v186, 1.0
	v_rcp_f32_e32 v206, v187
	s_nop 0
	v_fma_f32 v207, -v187, v206, 1.0
	v_fmac_f32_e32 v206, v207, v206
	v_div_scale_f32 v207, vcc, 1.0, v186, 1.0
	v_mul_f32_e32 v218, v207, v206
	v_fma_f32 v220, -v187, v218, v207
	v_fmac_f32_e32 v218, v220, v206
	v_fma_f32 v187, -v187, v218, v207
	v_div_fmas_f32 v187, v187, v206, v218
	v_div_fixup_f32 v220, v187, v186, 1.0
	v_pk_mul_f32 v[184:185], v[220:221], v[184:185] op_sel_hi:[0,1]
	v_pk_mul_f32 v[184:185], v[4:5], v[184:185]
	v_pk_add_f32 v[206:207], v[150:151], 1.0 op_sel_hi:[1,0]
	v_pk_mul_f32 v[186:187], v[220:221], v[208:209] op_sel_hi:[0,1]
	v_pk_fma_f32 v[206:207], v[206:207], v[184:185], v[162:163]
	v_mov_b32_e32 v184, v213
	v_mov_b32_e32 v185, v215
	v_pk_mul_f32 v[186:187], v[2:3], v[186:187]
	v_pk_add_f32 v[208:209], v[148:149], 1.0 op_sel_hi:[1,0]
	v_pk_mul_f32 v[184:185], v[220:221], v[184:185] op_sel_hi:[0,1]
	v_mov_b32_e32 v213, v214
	v_pk_fma_f32 v[208:209], v[208:209], v[186:187], v[160:161]
	v_pk_mul_f32 v[186:187], v[220:221], v[212:213] op_sel_hi:[0,1]
	v_pk_mul_f32 v[184:185], v[8:9], v[184:185]
	v_pk_add_f32 v[212:213], v[154:155], 1.0 op_sel_hi:[1,0]
	v_pk_mul_f32 v[186:187], v[6:7], v[186:187]
	v_pk_add_f32 v[214:215], v[152:153], 1.0 op_sel_hi:[1,0]
	v_pk_fma_f32 v[212:213], v[212:213], v[184:185], v[158:159]
	v_pk_mul_f32 v[184:185], v[220:221], v[216:217] op_sel_hi:[0,1]
	v_pk_fma_f32 v[214:215], v[214:215], v[186:187], v[156:157]
	v_pk_mul_f32 v[186:187], v[220:221], v[210:211] op_sel_hi:[0,1]
	v_pk_mul_f32 v[184:185], v[12:13], v[184:185]
	v_pk_add_f32 v[210:211], v[166:167], 1.0 op_sel_hi:[1,0]
	v_pk_mul_f32 v[186:187], v[10:11], v[186:187]
	v_pk_add_f32 v[216:217], v[164:165], 1.0 op_sel_hi:[1,0]
	v_pk_fma_f32 v[210:211], v[210:211], v[184:185], v[170:171]
	v_pk_mul_f32 v[184:185], v[222:223], v[220:221] op_sel_hi:[1,0]
	v_mov_b32_e32 v218, v221
	v_pk_fma_f32 v[216:217], v[216:217], v[186:187], v[168:169]
	v_pk_mul_f32 v[186:187], v[218:219], v[220:221] op_sel_hi:[1,0]
	v_pk_mul_f32 v[218:219], v[16:17], v[184:185]
	v_pk_add_f32 v[184:185], v[174:175], 1.0 op_sel_hi:[1,0]
	v_pk_mul_f32 v[220:221], v[14:15], v[186:187]
	v_pk_add_f32 v[186:187], v[172:173], 1.0 op_sel_hi:[1,0]
	v_pk_fma_f32 v[218:219], v[184:185], v[218:219], v[178:179]
	v_max_f32_e64 v184, |v208|, |v209|
	v_max_f32_e64 v185, |v206|, |v207|
	v_pk_fma_f32 v[220:221], v[186:187], v[220:221], v[176:177]
	v_max3_f32 v184, v184, 0, v185
	v_max_f32_e64 v185, |v214|, |v215|
	v_max_f32_e64 v186, |v212|, |v213|
	v_max3_f32 v184, v184, v185, v186
	v_max_f32_e64 v185, |v216|, |v217|
	v_max_f32_e64 v186, |v210|, |v211|
	v_max3_f32 v184, v184, v185, v186
	v_max_f32_e64 v185, |v220|, |v221|
	v_max_f32_e64 v186, |v218|, |v219|
	v_max3_f32 v184, v184, v185, v186
	s_waitcnt lgkmcnt(0)
	s_nop 1
	v_max_f32_dpp v184, v184, v184 quad_perm:[1,0,3,2] row_mask:0xf bank_mask:0xf
	s_nop 1
	v_max_f32_dpp v184, v184, v184 quad_perm:[2,3,0,1] row_mask:0xf bank_mask:0xf
	s_nop 1
	v_max_f32_dpp v184, v184, v184 row_half_mirror row_mask:0xf bank_mask:0xf
	s_nop 1
	v_max_f32_dpp v184, v184, v184 row_mirror row_mask:0xf bank_mask:0xf
	s_nop 1
	v_readlane_b32 s98, v184, 0
	v_readlane_b32 s99, v184, 16
	v_readlane_b32 s100, v184, 32
	v_readlane_b32 s101, v184, 48
	s_nop 1
	v_mov_b32_e32 v185, s99
	v_max_f32_e32 v185, s98, v185
	v_mov_b32_e32 v184, s101
	v_max_f32_e32 v184, s100, v184
	v_max_f32_e32 v222, v185, v184
	v_div_scale_f32 v184, s[2:3], v222, v222, s10
	v_rcp_f32_e32 v185, v184
	v_cmp_lt_f32_e64 s[0:1], 0, v222
	v_fma_f32 v186, -v184, v185, 1.0
	v_fmac_f32_e32 v185, v186, v185
	v_div_scale_f32 v186, vcc, s10, v222, s10
	v_mul_f32_e32 v187, v186, v185
	v_fma_f32 v223, -v184, v187, v186
	v_fmac_f32_e32 v187, v223, v185
	v_fma_f32 v184, -v184, v187, v186
	v_div_fmas_f32 v184, v184, v185, v187
	v_div_fixup_f32 v184, v184, v222, s10
	v_cndmask_b32_e64 v184, 0, v184, s[0:1]
	v_mul_f32_e32 v186, v209, v184
	v_mul_f32_e32 v185, v208, v184
	v_rndne_f32_e32 v186, v186
	v_mul_f32_e32 v187, v206, v184
	v_mul_f32_e32 v223, v207, v184
	v_rndne_f32_e32 v185, v185
	v_cvt_i32_f32_e32 v186, v186
	v_rndne_f32_e32 v187, v187
	v_rndne_f32_e32 v223, v223
	v_cvt_i32_f32_e32 v185, v185
	v_cvt_i32_f32_sdwa v187, v187 dst_sel:WORD_1 dst_unused:UNUSED_PAD src0_sel:DWORD
	v_cvt_i32_f32_e32 v223, v223
	v_lshlrev_b32_e32 v186, 8, v186
	s_mov_b32 s0, 0x40c0c00
	v_and_b32_e32 v186, 0xff00, v186
	v_and_b32_e32 v187, 0xff0000, v187
	v_perm_b32 v185, v223, v185, s0
	v_or3_b32 v185, v185, v186, v187
	v_mul_f32_e32 v186, v215, v184
	global_store_dword v[194:195], v185, off offset:-512
	v_mul_f32_e32 v185, v214, v184
	v_rndne_f32_e32 v186, v186
	v_mul_f32_e32 v187, v212, v184
	v_mul_f32_e32 v223, v213, v184
	v_rndne_f32_e32 v185, v185
	v_cvt_i32_f32_e32 v186, v186
	v_rndne_f32_e32 v187, v187
	v_rndne_f32_e32 v223, v223
	v_cvt_i32_f32_e32 v185, v185
	v_cvt_i32_f32_sdwa v187, v187 dst_sel:WORD_1 dst_unused:UNUSED_PAD src0_sel:DWORD
	v_cvt_i32_f32_e32 v223, v223
	v_lshlrev_b32_e32 v186, 8, v186
	v_and_b32_e32 v186, 0xff00, v186
	v_and_b32_e32 v187, 0xff0000, v187
	v_perm_b32 v185, v223, v185, s0
	v_or3_b32 v185, v185, v186, v187
	v_mul_f32_e32 v186, v217, v184
	global_store_dword v[194:195], v185, off offset:-256
	v_mul_f32_e32 v185, v216, v184
	v_rndne_f32_e32 v186, v186
	v_mul_f32_e32 v187, v210, v184
	v_mul_f32_e32 v223, v211, v184
	v_rndne_f32_e32 v185, v185
	v_cvt_i32_f32_e32 v186, v186
	v_rndne_f32_e32 v187, v187
	v_rndne_f32_e32 v223, v223
	v_cvt_i32_f32_e32 v185, v185
	v_cvt_i32_f32_sdwa v187, v187 dst_sel:WORD_1 dst_unused:UNUSED_PAD src0_sel:DWORD
	v_cvt_i32_f32_e32 v223, v223
	v_lshlrev_b32_e32 v186, 8, v186
	v_and_b32_e32 v186, 0xff00, v186
	v_and_b32_e32 v187, 0xff0000, v187
	v_perm_b32 v185, v223, v185, s0
	v_or3_b32 v185, v185, v186, v187
	v_mul_f32_e32 v186, v221, v184
	global_store_dword v[194:195], v185, off
	v_mul_f32_e32 v185, v220, v184
	v_rndne_f32_e32 v186, v186
	v_mul_f32_e32 v187, v218, v184
	v_mul_f32_e32 v184, v219, v184
	v_rndne_f32_e32 v185, v185
	v_cvt_i32_f32_e32 v186, v186
	v_rndne_f32_e32 v187, v187
	v_rndne_f32_e32 v184, v184
	v_cvt_i32_f32_e32 v185, v185
	v_cvt_i32_f32_sdwa v187, v187 dst_sel:WORD_1 dst_unused:UNUSED_PAD src0_sel:DWORD
	v_cvt_i32_f32_e32 v184, v184
	v_lshlrev_b32_e32 v186, 8, v186
	v_and_b32_e32 v186, 0xff00, v186
	v_and_b32_e32 v187, 0xff0000, v187
	v_perm_b32 v184, v184, v185, s0
	v_or3_b32 v184, v184, v186, v187
	global_store_dword v[194:195], v184, off offset:256
	s_and_saveexec_b64 s[0:1], s[36:37]
	s_cbranch_execz .LBB0_1219
	v_mul_f32_e32 v184, 0x3c010204, v222
	global_store_dword v[204:205], v184, off
